# diff-attention steps: scalar 32-term row-sum chain replaced by 15 v_pk_add_f32 on a register pair + 1 add
# baseline (speedup 1.0000x reference)
; #define WAIT_BAR(N) asm volatile("s_waitcnt vmcnt(" #N ") lgkmcnt(0)\n\ts_barrier":::"memory")
;   #define DMA_V(t,slot) glds16(vsrc+(long)(t)*KVBLK*PQ,(unsigned)__builtin_amdgcn_readfirstlane(vdst+(slot)))
;   #define CMASK(P0,P1,t) do{int jb_=(t)-(NT-4); if(jb_>=0)cmask(P0,P1,jb_,qrel,hi);}while(0)
;   #define ROT() do{sl_prev=sl_cur;sl_cur=sl_next;sl_next=(sl_next==(NSLOT-1)*SLOTB)?0:sl_next+SLOTB;}while(0)
;   #define PKW(P,B) cvtpk_s(P[B],P[B+1])
;   #define CMASK(P0,P1,t) do{}while(0)
;   #define CMASK(P0,P1,t) do{int jb_=(t)-(NT-4); if(jb_>=0)cmask(P0,P1,jb_,qrel,hi);}while(0)
; #define WAIT_BAR(N) asm volatile("s_waitcnt vmcnt(" #N ") lgkmcnt(0)\n\ts_barrier":::"memory")
;   #define DMA_V(t,slot) do{ glds16(vsrc+(long)(t)*KVBLK*PQ,(unsigned)__builtin_amdgcn_readfirstlane(vdst+2*(slot))); glds16(vsrc+(long)(t)*KVBLK*PQ+64,(unsigned)__builtin_amdgcn_readfirstlane(vdst+2*(slot)+8192)); }while(0)
;   #define CMASK(P0,P1,t) do{int jb_=(t)-(NT-4); if(jb_>=0)cmask(P0,P1,jb_,qrel,hi);}while(0)
;   #define ROT() do{sl_prev=sl_cur;sl_cur=sl_next;sl_next=(sl_next==(NSLOT-1)*SLOTB)?0:sl_next+SLOTB;}while(0)
;   #define PKW(P,B) cvtpk_s(P[B],P[B+1])
; template<int THRL> __device__ __forceinline__ void attn_unit2(int b,int qb,const bf16*Q,const bf16*__restrict__ K,const bf16*__restrict__ V,bf16*O,char*shm,int tid_in){
;     ...
;   WAIT_BAR(4);
;   qkt(c0,c1,Kbase,qr,zero16,r32,hi);asm volatile("s_nop 15\n\ts_nop 7":"+v"(c0),"+v"(c1));CMASK(c0,c1,0);
;   { const float rm=rowmax(c0,c1); mhat=rm;
;     _Pragma("unroll") for(int r=0;r<16;++r){c0[r]=__builtin_amdgcn_exp2f(c0[r]-rm);c1[r]=__builtin_amdgcn_exp2f(c1[r]-rm);}
;     float sacc=c0[0]+c0[1]; _Pragma("unroll") for(int r=2;r<16;++r)sacc+=c0[r]; _Pragma("unroll") for(int r=0;r<16;++r)sacc+=c1[r]; l_reg=sacc;
;     pa0=(u32x4){PKW(c0,0),PKW(c0,2),PKW(c0,4),PKW(c0,6)};pa1=(u32x4){PKW(c0,8),PKW(c0,10),PKW(c0,12),PKW(c0,14)};pa2=(u32x4){PKW(c1,0),PKW(c1,2),PKW(c1,4),PKW(c1,6)};pa3=(u32x4){PKW(c1,8),PKW(c1,10),PKW(c1,12),PKW(c1,14)}; }
;   WAIT_BAR(0);
;   DMA_V(1,SLOTB);
;   ROT();
;   kfa[0]=*(const __attribute__((address_space(3))) bf16x8*)(kp0+sl_cur);      kfa[1]=*(const __attribute__((address_space(3))) bf16x8*)(kp0+sl_cur+512);
;   kfa[2]=*(const __attribute__((address_space(3))) bf16x8*)(kp0+sl_cur+2048); kfa[3]=*(const __attribute__((address_space(3))) bf16x8*)(kp0+sl_cur+2560);
;   WAIT_BAR(2);
.LBB0_563:
	v_lshlrev_b32_e32 v37, 1, v3
	v_and_b32_e32 v37, 32, v37
	v_lshlrev_b32_e32 v38, 4, v3
	v_add3_u32 v36, 0, v37, v36
	v_lshlrev_b32_e32 v37, 8, v228
	v_and_b32_e32 v38, 0xc0, v38
	v_add3_u32 v225, v36, v37, v38
	v_max3_f32 v36, v4, v5, v20
	v_max3_f32 v37, v6, v7, v21
	s_and_b32 s9, s8, 0x3fffffc0
	v_max3_f32 v36, v36, v22, v23
	v_max3_f32 v37, v37, v10, v11
	s_lshl_b32 s9, s9, 2
	v_max3_f32 v36, v36, v8, v9
	v_max3_f32 v37, v37, v26, v27
	s_add_i32 s10, s22, 0x100
	v_max3_f32 v36, v36, v24, v25
	v_max3_f32 v37, v37, v14, v15
	s_add_i32 s17, s9, 0
	v_max3_f32 v36, v36, v12, v13
	v_max3_f32 v37, v37, v30, v31
	s_add_i32 s17, s17, 0x12000
	v_max3_f32 v36, v36, v28, v29
	v_max3_f32 v37, v37, v18, v19
	s_lshr_b32 s20, s10, 6
	v_max3_f32 v36, v36, v16, v17
	v_max3_f32 v37, v37, v34, v35
	s_cmp_lg_u32 0, -1
	v_max3_f32 v36, v36, v32, v33
	s_cselect_b32 s9, 0, 0
	v_max_f32_e32 v36, v36, v37
	s_waitcnt vmcnt(0) lgkmcnt(0)
	s_barrier
	s_mov_b64 s[10:11], 0x90000
	v_mov_b32_e32 v37, v36
	s_nop 1
	v_permlane32_swap_b32_e32 v36, v37
	v_max_f32_e32 v206, v36, v37
	s_add_i32 s3, s9, s3
	v_sub_f32_e32 v4, v4, v206
	v_sub_f32_e32 v5, v5, v206
	v_exp_f32_e32 v4, v4
	v_exp_f32_e32 v5, v5
	v_sub_f32_e32 v6, v6, v206
	v_exp_f32_e32 v6, v6
	v_sub_f32_e32 v7, v7, v206
	v_exp_f32_e32 v7, v7
	v_sub_f32_e32 v8, v8, v206
	v_exp_f32_e32 v8, v8
	v_sub_f32_e32 v9, v9, v206
	v_exp_f32_e32 v9, v9
	v_sub_f32_e32 v10, v10, v206
	v_exp_f32_e32 v10, v10
	v_sub_f32_e32 v11, v11, v206
	v_exp_f32_e32 v11, v11
	v_sub_f32_e32 v12, v12, v206
	v_pk_add_f32 v[242:243], v[4:5], v[6:7]
	v_exp_f32_e32 v12, v12
	v_sub_f32_e32 v13, v13, v206
	v_exp_f32_e32 v13, v13
	v_sub_f32_e32 v14, v14, v206
	v_pk_add_f32 v[242:243], v[242:243], v[8:9]
	v_exp_f32_e32 v14, v14
	v_sub_f32_e32 v15, v15, v206
	v_exp_f32_e32 v15, v15
	v_sub_f32_e32 v16, v16, v206
	v_pk_add_f32 v[242:243], v[242:243], v[10:11]
	v_exp_f32_e32 v16, v16
	v_sub_f32_e32 v17, v17, v206
	v_exp_f32_e32 v17, v17
	v_sub_f32_e32 v18, v18, v206
	v_pk_add_f32 v[242:243], v[242:243], v[12:13]
	v_exp_f32_e32 v18, v18
	v_sub_f32_e32 v19, v19, v206
	v_sub_f32_e32 v20, v20, v206
	v_exp_f32_e32 v19, v19
	v_pk_add_f32 v[242:243], v[242:243], v[14:15]
	v_exp_f32_e32 v20, v20
	v_sub_f32_e32 v21, v21, v206
	v_exp_f32_e32 v21, v21
	v_sub_f32_e32 v22, v22, v206
	v_pk_add_f32 v[242:243], v[242:243], v[16:17]
	v_exp_f32_e32 v22, v22
	v_sub_f32_e32 v23, v23, v206
	v_exp_f32_e32 v23, v23
	v_sub_f32_e32 v24, v24, v206
	v_pk_add_f32 v[242:243], v[242:243], v[18:19]
	v_exp_f32_e32 v24, v24
	v_sub_f32_e32 v25, v25, v206
	v_exp_f32_e32 v25, v25
	v_sub_f32_e32 v26, v26, v206
	v_pk_add_f32 v[242:243], v[242:243], v[20:21]
	v_exp_f32_e32 v26, v26
	v_sub_f32_e32 v27, v27, v206
	v_exp_f32_e32 v27, v27
	v_sub_f32_e32 v28, v28, v206
	v_pk_add_f32 v[242:243], v[242:243], v[22:23]
	v_exp_f32_e32 v28, v28
	v_sub_f32_e32 v29, v29, v206
	v_exp_f32_e32 v29, v29
	v_sub_f32_e32 v30, v30, v206
	v_pk_add_f32 v[242:243], v[242:243], v[24:25]
	v_exp_f32_e32 v30, v30
	v_sub_f32_e32 v31, v31, v206
	v_cvt_pk_bf16_f32 v142, v4, v5
	v_lshl_add_u64 v[4:5], v[0:1], 0, s[10:11]
	s_add_i32 s9, s3, 0xa000
	s_mov_b32 s10, m0
	s_mov_b32 m0, s9
	s_nop 0
	global_load_lds_dwordx4 v[4:5], off
	s_mov_b32 m0, s10
	v_exp_f32_e32 v31, v31
	v_sub_f32_e32 v32, v32, v206
	v_pk_add_f32 v[242:243], v[242:243], v[26:27]
	s_mov_b64 s[10:11], 0x90080
	v_exp_f32_e32 v32, v32
	v_sub_f32_e32 v33, v33, v206
	v_lshl_add_u64 v[0:1], v[0:1], 0, s[10:11]
	s_add_i32 s3, s3, 0xc000
	s_mov_b32 s9, m0
	s_mov_b32 m0, s3
	s_nop 0
	global_load_lds_dwordx4 v[0:1], off
	s_mov_b32 m0, s9
	v_exp_f32_e32 v33, v33
	v_sub_f32_e32 v34, v34, v206
	v_pk_add_f32 v[242:243], v[242:243], v[28:29]
	ds_read_b128 v[166:169], v224 offset:8192
	ds_read_b128 v[162:165], v224 offset:8704
	ds_read_b128 v[174:177], v224 offset:10240
	ds_read_b128 v[170:173], v224 offset:10752
	v_exp_f32_e32 v34, v34
	v_sub_f32_e32 v35, v35, v206
	v_exp_f32_e32 v35, v35
	v_pk_add_f32 v[242:243], v[242:243], v[30:31]
	v_pk_add_f32 v[242:243], v[242:243], v[32:33]
	s_waitcnt vmcnt(2) lgkmcnt(0)
	s_barrier
	v_and_b32_e32 v0, 3, v3
	s_mov_b32 s8, 1
	v_pk_add_f32 v[242:243], v[242:243], v[34:35]
	v_add_f32_e32 v227, v242, v243
	v_cvt_pk_bf16_f32 v143, v6, v7
	v_cvt_pk_bf16_f32 v144, v8, v9
	v_cvt_pk_bf16_f32 v145, v10, v11
	v_cvt_pk_bf16_f32 v138, v12, v13
	v_cvt_pk_bf16_f32 v139, v14, v15
	v_cvt_pk_bf16_f32 v140, v16, v17
	v_cvt_pk_bf16_f32 v141, v18, v19
	v_cvt_pk_bf16_f32 v134, v20, v21
	v_cvt_pk_bf16_f32 v135, v22, v23
	v_cvt_pk_bf16_f32 v136, v24, v25
	v_cvt_pk_bf16_f32 v137, v26, v27
	v_cvt_pk_bf16_f32 v130, v28, v29
	v_cvt_pk_bf16_f32 v131, v30, v31
	v_cvt_pk_bf16_f32 v132, v32, v33
	v_cvt_pk_bf16_f32 v133, v34, v35
	s_mov_b32 s24, 0
	s_andn2_b64 vcc, exec, s[6:7]
	v_lshlrev_b32_e32 v226, 4, v228
	s_mul_hi_i32 s25, s2, 0x1200000
	s_mul_i32 s26, s2, 0x1200000
	v_lshlrev_b32_e32 v196, 4, v0
	s_cbranch_vccnz .LBB0_579
	s_lshl_b64 s[6:7], s[4:5], 1
	s_add_u32 s6, s6, s0
	s_addc_u32 s7, s7, s1
	s_add_u32 s6, s6, s26
	v_mov_b32_e32 v197, v2
	s_addc_u32 s7, s7, s25
	v_lshl_add_u64 v[0:1], s[6:7], 0, v[196:197]
	v_mov_b32_e32 v195, v2
	v_readlane_b32 s6, v254, 27
	v_lshl_add_u64 v[0:1], v[0:1], 0, v[194:195]
	v_readlane_b32 s7, v254, 28
	v_mov_b32_e32 v14, v2
	v_mov_b32_e32 v15, v2
	v_lshl_add_u64 v[208:209], s[6:7], 0, v[0:1]
	v_mov_b32_e32 v0, v2
	v_mov_b32_e32 v1, v2
	v_mov_b32_e32 v3, v2
	v_mov_b32_e32 v4, v2
	v_mov_b32_e32 v5, v2
	v_mov_b32_e32 v6, v2
	v_mov_b32_e32 v7, v2
	v_mov_b32_e32 v8, v2
	v_mov_b32_e32 v9, v2
	v_mov_b32_e32 v10, v2
	v_mov_b32_e32 v11, v2
	v_mov_b32_e32 v12, v2
	v_mov_b32_e32 v13, v2
	v_mov_b64_e32 v[78:79], v[14:15]
	v_mov_b64_e32 v[62:63], v[14:15]
	v_mov_b64_e32 v[46:47], v[14:15]
	v_mov_b64_e32 v[30:31], v[14:15]
	v_cmp_gt_u32_e64 s[2:3], 32, v222
	v_lshl_add_u32 v229, v221, 2, s17
	s_movk_i32 s24, 0x4000
	s_movk_i32 s29, 0x2000
	s_mov_b32 s8, 0
	s_mov_b32 s28, 6
	s_mov_b64 s[6:7], 0
	v_mov_b64_e32 v[76:77], v[12:13]
	v_mov_b64_e32 v[74:75], v[10:11]
	v_mov_b64_e32 v[72:73], v[8:9]
	v_mov_b64_e32 v[70:71], v[6:7]
	v_mov_b64_e32 v[68:69], v[4:5]
	v_mov_b64_e32 v[66:67], v[2:3]
	v_mov_b64_e32 v[64:65], v[0:1]
	v_mov_b64_e32 v[60:61], v[12:13]
	v_mov_b64_e32 v[58:59], v[10:11]
	v_mov_b64_e32 v[56:57], v[8:9]
	v_mov_b64_e32 v[54:55], v[6:7]
	v_mov_b64_e32 v[52:53], v[4:5]
	v_mov_b64_e32 v[50:51], v[2:3]
	v_mov_b64_e32 v[48:49], v[0:1]
	v_mov_b64_e32 v[44:45], v[12:13]
	v_mov_b64_e32 v[42:43], v[10:11]
	v_mov_b64_e32 v[40:41], v[8:9]
	v_mov_b64_e32 v[38:39], v[6:7]
	v_mov_b64_e32 v[36:37], v[4:5]
	v_mov_b64_e32 v[34:35], v[2:3]
	v_mov_b64_e32 v[32:33], v[0:1]
	v_mov_b64_e32 v[28:29], v[12:13]
	v_mov_b64_e32 v[26:27], v[10:11]
	v_mov_b64_e32 v[24:25], v[8:9]
	v_mov_b64_e32 v[22:23], v[6:7]
	v_mov_b64_e32 v[20:21], v[4:5]
	v_mov_b64_e32 v[18:19], v[2:3]
	v_mov_b64_e32 v[16:17], v[0:1]

.LBB0_566:
	s_waitcnt lgkmcnt(14)
	v_mfma_f32_32x32x16_bf16 v[64:79], v[142:145], v[8:11], v[64:79]
	ds_read_b64_tr_b16 v[112:113], v3 offset:32768
	ds_read_b64_tr_b16 v[114:115], v3 offset:33280
	v_exp_f32_e32 v96, v96
	v_exp_f32_e32 v97, v97
	v_exp_f32_e32 v98, v98
	v_exp_f32_e32 v99, v99
	s_waitcnt lgkmcnt(14)
	v_mfma_f32_32x32x16_bf16 v[48:63], v[142:145], v[4:7], v[48:63]
	ds_read_b64_tr_b16 v[186:187], v3 offset:36864
	ds_read_b64_tr_b16 v[188:189], v3 offset:37376
	v_exp_f32_e32 v100, v100
	v_exp_f32_e32 v101, v101
	v_exp_f32_e32 v102, v102
	v_exp_f32_e32 v103, v103
	v_add_u32_e32 v192, s24, v224
	ds_read_b128 v[8:11], v192
	ds_read_b128 v[4:7], v192 offset:512
	s_waitcnt lgkmcnt(14)
	v_mfma_f32_32x32x16_bf16 v[64:79], v[138:141], v[12:15], v[64:79]
	ds_read_b64_tr_b16 v[230:231], v3 offset:33792
	ds_read_b64_tr_b16 v[232:233], v3 offset:34304
	v_exp_f32_e32 v104, v104
	v_exp_f32_e32 v105, v105
	v_exp_f32_e32 v106, v106
	v_exp_f32_e32 v107, v107
	ds_read_b128 v[162:165], v192 offset:2048
	ds_read_b128 v[12:15], v192 offset:2560
	v_mfma_f32_32x32x16_bf16 v[48:63], v[138:141], v[182:185], v[48:63]
	ds_read_b64_tr_b16 v[182:183], v3 offset:37888
	ds_read_b64_tr_b16 v[184:185], v3 offset:38400
	v_exp_f32_e32 v108, v108
	v_exp_f32_e32 v109, v109
	v_exp_f32_e32 v110, v110
	v_exp_f32_e32 v111, v111
	s_waitcnt lgkmcnt(14)
	v_mfma_f32_32x32x16_bf16 v[64:79], v[134:137], v[178:181], v[64:79]
	ds_read_b64_tr_b16 v[178:179], v3 offset:34816
	ds_read_b64_tr_b16 v[180:181], v3 offset:35328
	v_exp_f32_e32 v80, v80
	v_exp_f32_e32 v81, v81
	v_exp_f32_e32 v82, v82
	v_exp_f32_e32 v83, v83
	v_mfma_f32_32x32x16_bf16 v[48:63], v[134:137], v[174:177], v[48:63]
	ds_read_b64_tr_b16 v[174:175], v3 offset:38912
	ds_read_b64_tr_b16 v[176:177], v3 offset:39424
	v_exp_f32_e32 v84, v84
	v_exp_f32_e32 v85, v85
	v_exp_f32_e32 v86, v86
	v_exp_f32_e32 v87, v87
	v_mfma_f32_32x32x16_bf16 v[64:79], v[130:133], v[170:173], v[64:79]
	ds_read_b64_tr_b16 v[170:171], v3 offset:35840
	ds_read_b64_tr_b16 v[172:173], v3 offset:36352
	v_exp_f32_e32 v88, v88
	v_exp_f32_e32 v89, v89
	v_exp_f32_e32 v90, v90
	v_exp_f32_e32 v91, v91
	s_waitcnt lgkmcnt(14)
	v_mfma_f32_32x32x16_bf16 v[48:63], v[130:133], v[166:169], v[48:63]
	ds_read_b64_tr_b16 v[166:167], v3 offset:39936
	ds_read_b64_tr_b16 v[168:169], v3 offset:40448
	v_exp_f32_e32 v92, v92
	v_exp_f32_e32 v93, v93
	v_exp_f32_e32 v94, v94
	v_exp_f32_e32 v95, v95
	v_mfma_f32_32x32x16_bf16 v[32:47], v[142:145], v[112:115], v[32:47]
	v_pk_add_f32 v[242:243], v[96:97], v[98:99]
	v_pk_add_f32 v[242:243], v[242:243], v[100:101]
	v_cvt_pk_bf16_f32 v126, v96, v97
	v_cvt_pk_bf16_f32 v127, v98, v99
	v_mfma_f32_32x32x16_bf16 v[16:31], v[142:145], v[186:189], v[16:31]
	v_pk_add_f32 v[242:243], v[242:243], v[102:103]
	v_pk_add_f32 v[242:243], v[242:243], v[104:105]
	v_cvt_pk_bf16_f32 v128, v100, v101
	v_cvt_pk_bf16_f32 v129, v102, v103
	s_waitcnt lgkmcnt(12)
	v_mfma_f32_32x32x16_bf16 v[32:47], v[138:141], v[230:233], v[32:47]
	v_pk_add_f32 v[242:243], v[242:243], v[106:107]
	v_pk_add_f32 v[242:243], v[242:243], v[108:109]
	v_cvt_pk_bf16_f32 v122, v104, v105
	v_cvt_pk_bf16_f32 v123, v106, v107
	s_waitcnt lgkmcnt(8)
	v_mfma_f32_32x32x16_bf16 v[16:31], v[138:141], v[182:185], v[16:31]
	v_pk_add_f32 v[242:243], v[242:243], v[110:111]
	v_pk_add_f32 v[242:243], v[242:243], v[80:81]
	v_cvt_pk_bf16_f32 v124, v108, v109
	v_cvt_pk_bf16_f32 v125, v110, v111
	s_waitcnt lgkmcnt(6)
	v_mfma_f32_32x32x16_bf16 v[32:47], v[134:137], v[178:181], v[32:47]
	v_pk_add_f32 v[242:243], v[242:243], v[82:83]
	v_pk_add_f32 v[242:243], v[242:243], v[84:85]
	v_cvt_pk_bf16_f32 v118, v80, v81
	v_cvt_pk_bf16_f32 v119, v82, v83
	s_waitcnt lgkmcnt(4)
	v_mfma_f32_32x32x16_bf16 v[16:31], v[134:137], v[174:177], v[16:31]
	v_pk_add_f32 v[242:243], v[242:243], v[86:87]
	v_pk_add_f32 v[242:243], v[242:243], v[88:89]
	v_cvt_pk_bf16_f32 v120, v84, v85
	v_cvt_pk_bf16_f32 v121, v86, v87
	s_waitcnt lgkmcnt(2)
	v_mfma_f32_32x32x16_bf16 v[32:47], v[130:133], v[170:173], v[32:47]
	v_pk_add_f32 v[242:243], v[242:243], v[90:91]
	v_pk_add_f32 v[242:243], v[242:243], v[92:93]
	v_cvt_pk_bf16_f32 v114, v88, v89
	v_cvt_pk_bf16_f32 v115, v90, v91
	s_waitcnt lgkmcnt(0)
	v_mfma_f32_32x32x16_bf16 v[16:31], v[130:133], v[166:169], v[16:31]
	v_pk_add_f32 v[242:243], v[242:243], v[94:95]
	v_add_f32_e32 v3, v242, v243
	v_cvt_pk_bf16_f32 v116, v92, v93
	v_cvt_pk_bf16_f32 v117, v94, v95
	s_waitcnt vmcnt(2) lgkmcnt(0)
	s_barrier
	s_andn2_b64 vcc, exec, s[8:9]
	v_add_u32_e32 v195, s17, v226
	s_cbranch_vccnz .LBB0_568
	s_waitcnt lgkmcnt(0)
	ds_read_b128 v[80:83], v195 offset:96
	ds_read_b128 v[84:87], v195 offset:64
	ds_read_b128 v[88:91], v195 offset:32
	ds_read_b128 v[92:95], v195
	s_waitcnt lgkmcnt(3)
	v_pk_mul_f32 v[76:77], v[76:77], v[80:81]
	s_waitcnt lgkmcnt(2)
	v_pk_mul_f32 v[72:73], v[72:73], v[84:85]
	s_waitcnt lgkmcnt(1)
	v_pk_mul_f32 v[68:69], v[68:69], v[88:89]
	v_pk_mul_f32 v[78:79], v[78:79], v[82:83]
	v_pk_mul_f32 v[74:75], v[74:75], v[86:87]
	v_pk_mul_f32 v[70:71], v[70:71], v[90:91]
	s_waitcnt lgkmcnt(0)
	v_pk_mul_f32 v[66:67], v[66:67], v[94:95]
	v_pk_mul_f32 v[64:65], v[64:65], v[92:93]
	v_pk_mul_f32 v[60:61], v[60:61], v[80:81]
	v_pk_mul_f32 v[56:57], v[56:57], v[84:85]
	v_pk_mul_f32 v[52:53], v[52:53], v[88:89]
	v_pk_mul_f32 v[62:63], v[62:63], v[82:83]
	v_pk_mul_f32 v[58:59], v[58:59], v[86:87]
	v_pk_mul_f32 v[54:55], v[54:55], v[90:91]
	v_pk_mul_f32 v[50:51], v[50:51], v[94:95]
	v_pk_mul_f32 v[48:49], v[48:49], v[92:93]
	v_pk_mul_f32 v[44:45], v[44:45], v[80:81]
	v_pk_mul_f32 v[40:41], v[40:41], v[84:85]
	v_pk_mul_f32 v[36:37], v[36:37], v[88:89]
	v_pk_mul_f32 v[46:47], v[46:47], v[82:83]
	v_pk_mul_f32 v[42:43], v[42:43], v[86:87]
	v_pk_mul_f32 v[38:39], v[38:39], v[90:91]
	v_pk_mul_f32 v[34:35], v[34:35], v[94:95]
	v_pk_mul_f32 v[32:33], v[32:33], v[92:93]
	v_pk_mul_f32 v[28:29], v[28:29], v[80:81]
	v_pk_mul_f32 v[24:25], v[24:25], v[84:85]
	v_pk_mul_f32 v[20:21], v[20:21], v[88:89]
	v_pk_mul_f32 v[30:31], v[30:31], v[82:83]
	v_pk_mul_f32 v[26:27], v[26:27], v[86:87]
	v_pk_mul_f32 v[22:23], v[22:23], v[90:91]
	v_pk_mul_f32 v[18:19], v[18:19], v[94:95]
	v_pk_mul_f32 v[16:17], v[16:17], v[92:93]

.LBB0_569:
	s_waitcnt lgkmcnt(14)
	v_mfma_f32_32x32x16_bf16 v[64:79], v[126:129], v[174:177], v[64:79]
	ds_read_b64_tr_b16 v[186:187], v130 offset:32768
	ds_read_b64_tr_b16 v[188:189], v130 offset:33280
	v_exp_f32_e32 v96, v80
	v_exp_f32_e32 v97, v81
	v_exp_f32_e32 v98, v98
	v_exp_f32_e32 v99, v99
	s_waitcnt lgkmcnt(14)
	v_mfma_f32_32x32x16_bf16 v[48:63], v[126:129], v[166:169], v[48:63]
	ds_read_b64_tr_b16 v[190:191], v130 offset:36864
	ds_read_b64_tr_b16 v[192:193], v130 offset:37376
	v_exp_f32_e32 v100, v100
	v_exp_f32_e32 v101, v101
	v_exp_f32_e32 v102, v102
	v_exp_f32_e32 v103, v103
	v_add_u32_e32 v80, s27, v224
	ds_read_b128 v[166:169], v80
	ds_read_b128 v[162:165], v80 offset:512
	s_waitcnt lgkmcnt(14)
	v_mfma_f32_32x32x16_bf16 v[64:79], v[122:125], v[170:173], v[64:79]
	ds_read_b64_tr_b16 v[230:231], v130 offset:33792
	ds_read_b64_tr_b16 v[232:233], v130 offset:34304
	v_exp_f32_e32 v104, v104
	v_exp_f32_e32 v105, v105
	v_exp_f32_e32 v106, v106
	v_exp_f32_e32 v107, v107
	ds_read_b128 v[174:177], v80 offset:2048
	ds_read_b128 v[170:173], v80 offset:2560
	v_mfma_f32_32x32x16_bf16 v[48:63], v[122:125], v[182:185], v[48:63]
	ds_read_b64_tr_b16 v[182:183], v130 offset:37888
	ds_read_b64_tr_b16 v[184:185], v130 offset:38400
	v_exp_f32_e32 v108, v108
	v_exp_f32_e32 v109, v109
	v_exp_f32_e32 v110, v110
	v_exp_f32_e32 v111, v111
	s_waitcnt lgkmcnt(14)
	v_mfma_f32_32x32x16_bf16 v[64:79], v[118:121], v[178:181], v[64:79]
	ds_read_b64_tr_b16 v[178:179], v130 offset:34816
	ds_read_b64_tr_b16 v[180:181], v130 offset:35328
	v_exp_f32_e32 v80, v0
	v_exp_f32_e32 v81, v1
	v_exp_f32_e32 v82, v82
	v_exp_f32_e32 v83, v83
	v_mfma_f32_32x32x16_bf16 v[48:63], v[118:121], v[12:15], v[48:63]
	ds_read_b64_tr_b16 v[12:13], v130 offset:38912
	ds_read_b64_tr_b16 v[14:15], v130 offset:39424
	v_exp_f32_e32 v84, v84
	v_exp_f32_e32 v85, v85
	v_exp_f32_e32 v86, v86
	v_exp_f32_e32 v87, v87
	v_mfma_f32_32x32x16_bf16 v[64:79], v[114:117], v[8:11], v[64:79]
	ds_read_b64_tr_b16 v[8:9], v130 offset:35840
	ds_read_b64_tr_b16 v[10:11], v130 offset:36352
	v_exp_f32_e32 v88, v88
	v_exp_f32_e32 v89, v89
	v_exp_f32_e32 v90, v90
	v_exp_f32_e32 v91, v91
	s_waitcnt lgkmcnt(14)
	v_mfma_f32_32x32x16_bf16 v[48:63], v[114:117], v[4:7], v[48:63]
	ds_read_b64_tr_b16 v[4:5], v130 offset:39936
	ds_read_b64_tr_b16 v[6:7], v130 offset:40448
	v_exp_f32_e32 v92, v92
	v_exp_f32_e32 v93, v93
	v_exp_f32_e32 v94, v94
	v_exp_f32_e32 v95, v95
	v_mfma_f32_32x32x16_bf16 v[32:47], v[126:129], v[186:189], v[32:47]
	v_pk_add_f32 v[242:243], v[96:97], v[98:99]
	v_pk_add_f32 v[242:243], v[242:243], v[100:101]
	v_cvt_pk_bf16_f32 v142, v96, v97
	v_cvt_pk_bf16_f32 v143, v98, v99
	v_mfma_f32_32x32x16_bf16 v[16:31], v[126:129], v[190:193], v[16:31]
	v_pk_add_f32 v[242:243], v[242:243], v[102:103]
	v_pk_add_f32 v[242:243], v[242:243], v[104:105]
	v_cvt_pk_bf16_f32 v144, v100, v101
	v_cvt_pk_bf16_f32 v145, v102, v103
	s_waitcnt lgkmcnt(12)
	v_mfma_f32_32x32x16_bf16 v[32:47], v[122:125], v[230:233], v[32:47]
	v_pk_add_f32 v[242:243], v[242:243], v[106:107]
	v_pk_add_f32 v[242:243], v[242:243], v[108:109]
	v_cvt_pk_bf16_f32 v138, v104, v105
	v_cvt_pk_bf16_f32 v139, v106, v107
	s_waitcnt lgkmcnt(8)
	v_mfma_f32_32x32x16_bf16 v[16:31], v[122:125], v[182:185], v[16:31]
	v_pk_add_f32 v[242:243], v[242:243], v[110:111]
	v_pk_add_f32 v[242:243], v[242:243], v[80:81]
	v_cvt_pk_bf16_f32 v140, v108, v109
	v_cvt_pk_bf16_f32 v141, v110, v111
	s_waitcnt lgkmcnt(6)
	v_mfma_f32_32x32x16_bf16 v[32:47], v[118:121], v[178:181], v[32:47]
	v_pk_add_f32 v[242:243], v[242:243], v[82:83]
	v_pk_add_f32 v[242:243], v[242:243], v[84:85]
	v_cvt_pk_bf16_f32 v134, v80, v81
	v_cvt_pk_bf16_f32 v135, v82, v83
	s_waitcnt lgkmcnt(4)
	v_mfma_f32_32x32x16_bf16 v[16:31], v[118:121], v[12:15], v[16:31]
	v_pk_add_f32 v[242:243], v[242:243], v[86:87]
	v_pk_add_f32 v[242:243], v[242:243], v[88:89]
	v_cvt_pk_bf16_f32 v136, v84, v85
	v_cvt_pk_bf16_f32 v137, v86, v87
	s_waitcnt lgkmcnt(2)
	v_mfma_f32_32x32x16_bf16 v[32:47], v[114:117], v[8:11], v[32:47]
	v_pk_add_f32 v[242:243], v[242:243], v[90:91]
	v_pk_add_f32 v[242:243], v[242:243], v[92:93]
	v_cvt_pk_bf16_f32 v130, v88, v89
	v_cvt_pk_bf16_f32 v131, v90, v91
	s_waitcnt lgkmcnt(0)
	v_mfma_f32_32x32x16_bf16 v[16:31], v[114:117], v[4:7], v[16:31]
	v_pk_add_f32 v[242:243], v[242:243], v[94:95]
	v_add_f32_e32 v0, v242, v243
	v_cvt_pk_bf16_f32 v132, v92, v93
	v_cvt_pk_bf16_f32 v133, v94, v95
	s_waitcnt vmcnt(2) lgkmcnt(0)
	s_barrier
	s_andn2_b64 vcc, exec, s[8:9]
	s_cbranch_vccnz .LBB0_571
	s_waitcnt lgkmcnt(0)
	ds_read_b128 v[4:7], v195 offset:96
	ds_read_b128 v[8:11], v195 offset:64
	ds_read_b128 v[12:15], v195 offset:32
	ds_read_b128 v[80:83], v195
	s_waitcnt lgkmcnt(3)
	v_pk_mul_f32 v[76:77], v[76:77], v[4:5]
	s_waitcnt lgkmcnt(2)
	v_pk_mul_f32 v[72:73], v[72:73], v[8:9]
	s_waitcnt lgkmcnt(1)
	v_pk_mul_f32 v[68:69], v[68:69], v[12:13]
	v_pk_mul_f32 v[78:79], v[78:79], v[6:7]
	v_pk_mul_f32 v[74:75], v[74:75], v[10:11]
	v_pk_mul_f32 v[70:71], v[70:71], v[14:15]
	s_waitcnt lgkmcnt(0)
	v_pk_mul_f32 v[66:67], v[66:67], v[82:83]
	v_pk_mul_f32 v[64:65], v[64:65], v[80:81]
	v_pk_mul_f32 v[60:61], v[60:61], v[4:5]
	v_pk_mul_f32 v[56:57], v[56:57], v[8:9]
	v_pk_mul_f32 v[52:53], v[52:53], v[12:13]
	v_pk_mul_f32 v[62:63], v[62:63], v[6:7]
	v_pk_mul_f32 v[58:59], v[58:59], v[10:11]
	v_pk_mul_f32 v[54:55], v[54:55], v[14:15]
	v_pk_mul_f32 v[50:51], v[50:51], v[82:83]
	v_pk_mul_f32 v[48:49], v[48:49], v[80:81]
	v_pk_mul_f32 v[44:45], v[44:45], v[4:5]
	v_pk_mul_f32 v[40:41], v[40:41], v[8:9]
	v_pk_mul_f32 v[36:37], v[36:37], v[12:13]
	v_pk_mul_f32 v[46:47], v[46:47], v[6:7]
	v_pk_mul_f32 v[42:43], v[42:43], v[10:11]
	v_pk_mul_f32 v[38:39], v[38:39], v[14:15]
	v_pk_mul_f32 v[34:35], v[34:35], v[82:83]
	v_pk_mul_f32 v[32:33], v[32:33], v[80:81]
	v_pk_mul_f32 v[28:29], v[28:29], v[4:5]
	v_pk_mul_f32 v[24:25], v[24:25], v[8:9]
	v_pk_mul_f32 v[20:21], v[20:21], v[12:13]
	v_pk_mul_f32 v[30:31], v[30:31], v[6:7]
	v_pk_mul_f32 v[26:27], v[26:27], v[10:11]
	v_pk_mul_f32 v[22:23], v[22:23], v[14:15]
	v_pk_mul_f32 v[18:19], v[18:19], v[82:83]
	v_pk_mul_f32 v[16:17], v[16:17], v[80:81]

.LBB0_583:
	s_waitcnt lgkmcnt(14)
	v_mfma_f32_32x32x16_bf16 v[64:79], v[142:145], v[178:181], v[64:79]
	ds_read_b64_tr_b16 v[146:147], v0 offset:32768
	ds_read_b64_tr_b16 v[148:149], v0 offset:33280
	v_exp_f32_e32 v96, v96
	v_exp_f32_e32 v97, v97
	v_exp_f32_e32 v98, v98
	v_exp_f32_e32 v99, v99
	s_waitcnt lgkmcnt(14)
	v_mfma_f32_32x32x16_bf16 v[48:63], v[142:145], v[166:169], v[48:63]
	ds_read_b64_tr_b16 v[150:151], v0 offset:36864
	ds_read_b64_tr_b16 v[152:153], v0 offset:37376
	v_exp_f32_e32 v100, v100
	v_exp_f32_e32 v101, v101
	v_exp_f32_e32 v102, v102
	v_exp_f32_e32 v103, v103
	s_waitcnt lgkmcnt(14)
	v_mfma_f32_32x32x16_bf16 v[64:79], v[138:141], v[162:165], v[64:79]
	ds_read_b64_tr_b16 v[154:155], v0 offset:33792
	ds_read_b64_tr_b16 v[156:157], v0 offset:34304
	v_exp_f32_e32 v104, v104
	v_exp_f32_e32 v105, v105
	v_exp_f32_e32 v106, v106
	v_exp_f32_e32 v107, v107
	s_waitcnt lgkmcnt(14)
	v_mfma_f32_32x32x16_bf16 v[48:63], v[138:141], v[158:161], v[48:63]
	ds_read_b64_tr_b16 v[158:159], v0 offset:37888
	ds_read_b64_tr_b16 v[160:161], v0 offset:38400
	v_exp_f32_e32 v108, v108
	v_exp_f32_e32 v109, v109
	v_exp_f32_e32 v110, v110
	v_exp_f32_e32 v111, v111
	s_waitcnt lgkmcnt(14)
	v_mfma_f32_32x32x16_bf16 v[64:79], v[134:137], v[112:115], v[64:79]
	ds_read_b64_tr_b16 v[112:113], v0 offset:34816
	ds_read_b64_tr_b16 v[114:115], v0 offset:35328
	v_exp_f32_e32 v80, v80
	v_exp_f32_e32 v81, v81
	v_exp_f32_e32 v82, v82
	v_exp_f32_e32 v83, v83
	s_waitcnt lgkmcnt(14)
	v_mfma_f32_32x32x16_bf16 v[48:63], v[134:137], v[12:15], v[48:63]
	ds_read_b64_tr_b16 v[12:13], v0 offset:38912
	ds_read_b64_tr_b16 v[14:15], v0 offset:39424
	v_exp_f32_e32 v84, v84
	v_exp_f32_e32 v85, v85
	v_exp_f32_e32 v86, v86
	v_exp_f32_e32 v87, v87
	s_waitcnt lgkmcnt(14)
	v_mfma_f32_32x32x16_bf16 v[64:79], v[130:133], v[8:11], v[64:79]
	ds_read_b64_tr_b16 v[8:9], v0 offset:35840
	ds_read_b64_tr_b16 v[10:11], v0 offset:36352
	v_exp_f32_e32 v88, v88
	v_exp_f32_e32 v89, v89
	v_exp_f32_e32 v90, v90
	v_exp_f32_e32 v91, v91
	s_waitcnt lgkmcnt(14)
	v_mfma_f32_32x32x16_bf16 v[48:63], v[130:133], v[4:7], v[48:63]
	ds_read_b64_tr_b16 v[4:5], v0 offset:39936
	ds_read_b64_tr_b16 v[6:7], v0 offset:40448
	v_exp_f32_e32 v92, v92
	v_exp_f32_e32 v93, v93
	v_exp_f32_e32 v94, v94
	v_exp_f32_e32 v95, v95
	s_waitcnt lgkmcnt(14)
	v_mfma_f32_32x32x16_bf16 v[32:47], v[142:145], v[146:149], v[32:47]
	v_pk_add_f32 v[242:243], v[96:97], v[98:99]
	v_pk_add_f32 v[242:243], v[242:243], v[100:101]
	v_cvt_pk_bf16_f32 v126, v96, v97
	v_cvt_pk_bf16_f32 v127, v98, v99
	s_waitcnt lgkmcnt(12)
	v_mfma_f32_32x32x16_bf16 v[16:31], v[142:145], v[150:153], v[16:31]
	v_pk_add_f32 v[242:243], v[242:243], v[102:103]
	v_pk_add_f32 v[242:243], v[242:243], v[104:105]
	v_cvt_pk_bf16_f32 v128, v100, v101
	v_cvt_pk_bf16_f32 v129, v102, v103
	s_waitcnt lgkmcnt(10)
	v_mfma_f32_32x32x16_bf16 v[32:47], v[138:141], v[154:157], v[32:47]
	v_pk_add_f32 v[242:243], v[242:243], v[106:107]
	v_pk_add_f32 v[242:243], v[242:243], v[108:109]
	v_cvt_pk_bf16_f32 v122, v104, v105
	v_cvt_pk_bf16_f32 v123, v106, v107
	s_waitcnt lgkmcnt(8)
	v_mfma_f32_32x32x16_bf16 v[16:31], v[138:141], v[158:161], v[16:31]
	v_pk_add_f32 v[242:243], v[242:243], v[110:111]
	v_pk_add_f32 v[242:243], v[242:243], v[80:81]
	v_cvt_pk_bf16_f32 v124, v108, v109
	v_cvt_pk_bf16_f32 v125, v110, v111
	s_waitcnt lgkmcnt(6)
	v_mfma_f32_32x32x16_bf16 v[32:47], v[134:137], v[112:115], v[32:47]
	v_pk_add_f32 v[242:243], v[242:243], v[82:83]
	v_pk_add_f32 v[242:243], v[242:243], v[84:85]
	v_cvt_pk_bf16_f32 v118, v80, v81
	v_cvt_pk_bf16_f32 v119, v82, v83
	s_waitcnt lgkmcnt(4)
	v_mfma_f32_32x32x16_bf16 v[16:31], v[134:137], v[12:15], v[16:31]
	v_pk_add_f32 v[242:243], v[242:243], v[86:87]
	v_pk_add_f32 v[242:243], v[242:243], v[88:89]
	v_cvt_pk_bf16_f32 v120, v84, v85
	v_cvt_pk_bf16_f32 v121, v86, v87
	s_waitcnt lgkmcnt(2)
	v_mfma_f32_32x32x16_bf16 v[32:47], v[130:133], v[8:11], v[32:47]
	v_pk_add_f32 v[242:243], v[242:243], v[90:91]
	v_pk_add_f32 v[242:243], v[242:243], v[92:93]
	v_cvt_pk_bf16_f32 v114, v88, v89
	v_cvt_pk_bf16_f32 v115, v90, v91
	s_waitcnt lgkmcnt(0)
	v_mfma_f32_32x32x16_bf16 v[16:31], v[130:133], v[4:7], v[16:31]
	v_pk_add_f32 v[242:243], v[242:243], v[94:95]
	v_add_f32_e32 v0, v242, v243
	v_cvt_pk_bf16_f32 v116, v92, v93
	v_cvt_pk_bf16_f32 v117, v94, v95
	s_andn2_b64 vcc, exec, s[0:1]
	s_cbranch_vccnz .LBB0_585
	s_waitcnt lgkmcnt(0)
	v_lshl_add_u32 v1, v220, 2, s17
	ds_read_b128 v[4:7], v1 offset:96
	ds_read_b128 v[8:11], v1 offset:64
	ds_read_b128 v[12:15], v1 offset:32
	ds_read_b128 v[80:83], v1
	s_waitcnt lgkmcnt(3)
	v_pk_mul_f32 v[78:79], v[78:79], v[6:7]
	s_waitcnt lgkmcnt(2)
	v_pk_mul_f32 v[74:75], v[74:75], v[10:11]
	s_waitcnt lgkmcnt(1)
	v_pk_mul_f32 v[70:71], v[70:71], v[14:15]
	s_waitcnt lgkmcnt(0)
	v_pk_mul_f32 v[66:67], v[66:67], v[82:83]
	v_pk_mul_f32 v[76:77], v[76:77], v[4:5]
	v_pk_mul_f32 v[72:73], v[72:73], v[8:9]
	v_pk_mul_f32 v[68:69], v[68:69], v[12:13]
	v_pk_mul_f32 v[64:65], v[64:65], v[80:81]
	v_pk_mul_f32 v[62:63], v[62:63], v[6:7]
	v_pk_mul_f32 v[58:59], v[58:59], v[10:11]
	v_pk_mul_f32 v[54:55], v[54:55], v[14:15]
	v_pk_mul_f32 v[50:51], v[50:51], v[82:83]
	v_pk_mul_f32 v[60:61], v[60:61], v[4:5]
	v_pk_mul_f32 v[56:57], v[56:57], v[8:9]
	v_pk_mul_f32 v[52:53], v[52:53], v[12:13]
	v_pk_mul_f32 v[48:49], v[48:49], v[80:81]
	v_pk_mul_f32 v[46:47], v[46:47], v[6:7]
	v_pk_mul_f32 v[42:43], v[42:43], v[10:11]
	v_pk_mul_f32 v[38:39], v[38:39], v[14:15]
	v_pk_mul_f32 v[34:35], v[34:35], v[82:83]
	v_pk_mul_f32 v[44:45], v[44:45], v[4:5]
	v_pk_mul_f32 v[40:41], v[40:41], v[8:9]
	v_pk_mul_f32 v[36:37], v[36:37], v[12:13]
	v_pk_mul_f32 v[32:33], v[32:33], v[80:81]
	v_pk_mul_f32 v[30:31], v[30:31], v[6:7]
	v_pk_mul_f32 v[26:27], v[26:27], v[10:11]
	v_pk_mul_f32 v[22:23], v[22:23], v[14:15]
	v_pk_mul_f32 v[18:19], v[18:19], v[82:83]
	v_pk_mul_f32 v[28:29], v[28:29], v[4:5]
	v_pk_mul_f32 v[24:25], v[24:25], v[8:9]
	v_pk_mul_f32 v[20:21], v[20:21], v[12:13]
	v_pk_mul_f32 v[16:17], v[16:17], v[80:81]

.LBB0_595:
	s_waitcnt lgkmcnt(14)
	v_mfma_f32_32x32x16_bf16 v[64:79], v[142:145], v[186:189], v[64:79]
	ds_read_b64_tr_b16 v[192:193], v118 offset:32768
	ds_read_b64_tr_b16 v[194:195], v118 offset:33280
	v_exp_f32_e32 v96, v96
	v_exp_f32_e32 v97, v97
	v_exp_f32_e32 v98, v98
	v_exp_f32_e32 v99, v99
	s_waitcnt lgkmcnt(14)
	v_mfma_f32_32x32x16_bf16 v[48:63], v[142:145], v[166:169], v[48:63]
	ds_read_b64_tr_b16 v[230:231], v118 offset:36864
	ds_read_b64_tr_b16 v[232:233], v118 offset:37376
	v_exp_f32_e32 v100, v100
	v_exp_f32_e32 v101, v101
	v_exp_f32_e32 v102, v102
	v_exp_f32_e32 v103, v103
	v_add_u32_e32 v186, s23, v224
	ds_read_b128 v[166:169], v186
	ds_read_b128 v[162:165], v186 offset:512
	s_waitcnt lgkmcnt(14)
	v_mfma_f32_32x32x16_bf16 v[64:79], v[138:141], v[182:185], v[64:79]
	ds_read_b64_tr_b16 v[182:183], v118 offset:33792
	ds_read_b64_tr_b16 v[184:185], v118 offset:34304
	v_exp_f32_e32 v104, v104
	v_exp_f32_e32 v105, v105
	v_exp_f32_e32 v106, v106
	v_exp_f32_e32 v107, v107
	ds_read_b128 v[174:177], v186 offset:2048
	ds_read_b128 v[170:173], v186 offset:2560
	v_mfma_f32_32x32x16_bf16 v[48:63], v[138:141], v[178:181], v[48:63]
	ds_read_b64_tr_b16 v[178:179], v118 offset:37888
	ds_read_b64_tr_b16 v[180:181], v118 offset:38400
	v_exp_f32_e32 v108, v108
	v_exp_f32_e32 v109, v109
	v_exp_f32_e32 v110, v110
	v_exp_f32_e32 v111, v111
	s_waitcnt lgkmcnt(14)
	v_mfma_f32_32x32x16_bf16 v[64:79], v[134:137], v[112:115], v[64:79]
	ds_read_b64_tr_b16 v[112:113], v118 offset:34816
	ds_read_b64_tr_b16 v[114:115], v118 offset:35328
	v_exp_f32_e32 v80, v80
	v_exp_f32_e32 v81, v81
	v_exp_f32_e32 v82, v82
	v_exp_f32_e32 v83, v83
	v_mfma_f32_32x32x16_bf16 v[48:63], v[134:137], v[12:15], v[48:63]
	ds_read_b64_tr_b16 v[12:13], v118 offset:38912
	ds_read_b64_tr_b16 v[14:15], v118 offset:39424
	v_exp_f32_e32 v84, v84
	v_exp_f32_e32 v85, v85
	v_exp_f32_e32 v86, v86
	v_exp_f32_e32 v87, v87
	v_mfma_f32_32x32x16_bf16 v[64:79], v[130:133], v[8:11], v[64:79]
	ds_read_b64_tr_b16 v[8:9], v118 offset:35840
	ds_read_b64_tr_b16 v[10:11], v118 offset:36352
	v_exp_f32_e32 v88, v88
	v_exp_f32_e32 v89, v89
	v_exp_f32_e32 v90, v90
	v_exp_f32_e32 v91, v91
	s_waitcnt lgkmcnt(14)
	v_mfma_f32_32x32x16_bf16 v[48:63], v[130:133], v[4:7], v[48:63]
	ds_read_b64_tr_b16 v[4:5], v118 offset:39936
	ds_read_b64_tr_b16 v[6:7], v118 offset:40448
	v_exp_f32_e32 v92, v92
	v_exp_f32_e32 v93, v93
	v_exp_f32_e32 v94, v94
	v_exp_f32_e32 v95, v95
	v_mfma_f32_32x32x16_bf16 v[32:47], v[142:145], v[192:195], v[32:47]
	v_pk_add_f32 v[242:243], v[96:97], v[98:99]
	v_pk_add_f32 v[242:243], v[242:243], v[100:101]
	v_cvt_pk_bf16_f32 v126, v96, v97
	v_cvt_pk_bf16_f32 v127, v98, v99
	v_mfma_f32_32x32x16_bf16 v[16:31], v[142:145], v[230:233], v[16:31]
	v_pk_add_f32 v[242:243], v[242:243], v[102:103]
	v_pk_add_f32 v[242:243], v[242:243], v[104:105]
	v_cvt_pk_bf16_f32 v128, v100, v101
	v_cvt_pk_bf16_f32 v129, v102, v103
	s_waitcnt lgkmcnt(12)
	v_mfma_f32_32x32x16_bf16 v[32:47], v[138:141], v[182:185], v[32:47]
	v_pk_add_f32 v[242:243], v[242:243], v[106:107]
	v_pk_add_f32 v[242:243], v[242:243], v[108:109]
	v_cvt_pk_bf16_f32 v122, v104, v105
	v_cvt_pk_bf16_f32 v123, v106, v107
	s_waitcnt lgkmcnt(8)
	v_mfma_f32_32x32x16_bf16 v[16:31], v[138:141], v[178:181], v[16:31]
	v_pk_add_f32 v[242:243], v[242:243], v[110:111]
	v_pk_add_f32 v[242:243], v[242:243], v[80:81]
	v_cvt_pk_bf16_f32 v124, v108, v109
	v_cvt_pk_bf16_f32 v125, v110, v111
	s_waitcnt lgkmcnt(6)
	v_mfma_f32_32x32x16_bf16 v[32:47], v[134:137], v[112:115], v[32:47]
	v_pk_add_f32 v[242:243], v[242:243], v[82:83]
	v_pk_add_f32 v[242:243], v[242:243], v[84:85]
	v_cvt_pk_bf16_f32 v118, v80, v81
	v_cvt_pk_bf16_f32 v119, v82, v83
	s_waitcnt lgkmcnt(4)
	v_mfma_f32_32x32x16_bf16 v[16:31], v[134:137], v[12:15], v[16:31]
	v_pk_add_f32 v[242:243], v[242:243], v[86:87]
	v_pk_add_f32 v[242:243], v[242:243], v[88:89]
	v_cvt_pk_bf16_f32 v120, v84, v85
	v_cvt_pk_bf16_f32 v121, v86, v87
	s_waitcnt lgkmcnt(2)
	v_mfma_f32_32x32x16_bf16 v[32:47], v[130:133], v[8:11], v[32:47]
	v_pk_add_f32 v[242:243], v[242:243], v[90:91]
	v_pk_add_f32 v[242:243], v[242:243], v[92:93]
	v_cvt_pk_bf16_f32 v114, v88, v89
	v_cvt_pk_bf16_f32 v115, v90, v91
	s_waitcnt lgkmcnt(0)
	v_mfma_f32_32x32x16_bf16 v[16:31], v[130:133], v[4:7], v[16:31]
	v_pk_add_f32 v[242:243], v[242:243], v[94:95]
	v_add_f32_e32 v113, v242, v243
	v_cvt_pk_bf16_f32 v116, v92, v93
	v_cvt_pk_bf16_f32 v117, v94, v95
	s_mov_b64 s[10:11], -1
	s_and_b64 vcc, exec, s[4:5]
	s_cbranch_vccz .LBB0_616
	s_waitcnt vmcnt(0) lgkmcnt(0)
	s_barrier
	s_cbranch_execz .LBB0_617

.LBB0_610:
	s_waitcnt lgkmcnt(14)
	v_mfma_f32_32x32x16_bf16 v[48:63], v[122:125], v[182:185], v[48:63]
	ds_read_b64_tr_b16 v[182:183], v130 offset:37888
	ds_read_b64_tr_b16 v[184:185], v130 offset:38400
	v_exp_f32_e32 v108, v108
	v_exp_f32_e32 v109, v109
	v_exp_f32_e32 v110, v110
	v_exp_f32_e32 v111, v111
	s_waitcnt lgkmcnt(14)
	v_mfma_f32_32x32x16_bf16 v[64:79], v[118:121], v[178:181], v[64:79]
	ds_read_b64_tr_b16 v[178:179], v130 offset:34816
	ds_read_b64_tr_b16 v[180:181], v130 offset:35328
	v_exp_f32_e32 v80, v80
	v_exp_f32_e32 v81, v81
	v_exp_f32_e32 v82, v82
	v_exp_f32_e32 v83, v83
	s_waitcnt lgkmcnt(14)
	v_mfma_f32_32x32x16_bf16 v[48:63], v[118:121], v[12:15], v[48:63]
	ds_read_b64_tr_b16 v[12:13], v130 offset:38912
	ds_read_b64_tr_b16 v[14:15], v130 offset:39424
	v_exp_f32_e32 v84, v84
	v_exp_f32_e32 v85, v85
	v_exp_f32_e32 v86, v86
	v_exp_f32_e32 v87, v87
	s_waitcnt lgkmcnt(14)
	v_mfma_f32_32x32x16_bf16 v[64:79], v[114:117], v[8:11], v[64:79]
	ds_read_b64_tr_b16 v[8:9], v130 offset:35840
	ds_read_b64_tr_b16 v[10:11], v130 offset:36352
	v_exp_f32_e32 v88, v88
	v_exp_f32_e32 v89, v89
	v_exp_f32_e32 v90, v90
	v_exp_f32_e32 v91, v91
	s_waitcnt lgkmcnt(14)
	v_mfma_f32_32x32x16_bf16 v[48:63], v[114:117], v[4:7], v[48:63]
	ds_read_b64_tr_b16 v[4:5], v130 offset:39936
	ds_read_b64_tr_b16 v[6:7], v130 offset:40448
	v_exp_f32_e32 v92, v92
	v_exp_f32_e32 v93, v93
	v_exp_f32_e32 v94, v94
	v_exp_f32_e32 v95, v95
	s_waitcnt lgkmcnt(14)
	v_mfma_f32_32x32x16_bf16 v[32:47], v[126:129], v[194:197], v[32:47]
	v_pk_add_f32 v[242:243], v[96:97], v[98:99]
	v_pk_add_f32 v[242:243], v[242:243], v[100:101]
	v_cvt_pk_bf16_f32 v142, v96, v97
	v_cvt_pk_bf16_f32 v143, v98, v99
	s_waitcnt lgkmcnt(12)
	v_mfma_f32_32x32x16_bf16 v[16:31], v[126:129], v[190:193], v[16:31]
	v_pk_add_f32 v[242:243], v[242:243], v[102:103]
	v_pk_add_f32 v[242:243], v[242:243], v[104:105]
	v_cvt_pk_bf16_f32 v144, v100, v101
	v_cvt_pk_bf16_f32 v145, v102, v103
	s_waitcnt lgkmcnt(10)
	v_mfma_f32_32x32x16_bf16 v[32:47], v[122:125], v[186:189], v[32:47]
	v_pk_add_f32 v[242:243], v[242:243], v[106:107]
	v_pk_add_f32 v[242:243], v[242:243], v[108:109]
	v_cvt_pk_bf16_f32 v138, v104, v105
	v_cvt_pk_bf16_f32 v139, v106, v107
	s_waitcnt lgkmcnt(8)
	v_mfma_f32_32x32x16_bf16 v[16:31], v[122:125], v[182:185], v[16:31]
	v_pk_add_f32 v[242:243], v[242:243], v[110:111]
	v_pk_add_f32 v[242:243], v[242:243], v[80:81]
	v_cvt_pk_bf16_f32 v140, v108, v109
	v_cvt_pk_bf16_f32 v141, v110, v111
	s_waitcnt lgkmcnt(6)
	v_mfma_f32_32x32x16_bf16 v[32:47], v[118:121], v[178:181], v[32:47]
	v_pk_add_f32 v[242:243], v[242:243], v[82:83]
	v_pk_add_f32 v[242:243], v[242:243], v[84:85]
	v_cvt_pk_bf16_f32 v134, v80, v81
	v_cvt_pk_bf16_f32 v135, v82, v83
	s_waitcnt lgkmcnt(4)
	v_mfma_f32_32x32x16_bf16 v[16:31], v[118:121], v[12:15], v[16:31]
	v_pk_add_f32 v[242:243], v[242:243], v[86:87]
	v_pk_add_f32 v[242:243], v[242:243], v[88:89]
	v_cvt_pk_bf16_f32 v136, v84, v85
	v_cvt_pk_bf16_f32 v137, v86, v87
	s_waitcnt lgkmcnt(2)
	v_mfma_f32_32x32x16_bf16 v[32:47], v[114:117], v[8:11], v[32:47]
	v_pk_add_f32 v[242:243], v[242:243], v[90:91]
	v_pk_add_f32 v[242:243], v[242:243], v[92:93]
	v_cvt_pk_bf16_f32 v130, v88, v89
	v_cvt_pk_bf16_f32 v131, v90, v91
	s_waitcnt lgkmcnt(0)
	v_mfma_f32_32x32x16_bf16 v[16:31], v[114:117], v[4:7], v[16:31]
	v_pk_add_f32 v[242:243], v[242:243], v[94:95]
	v_add_f32_e32 v4, v242, v243
	v_cvt_pk_bf16_f32 v132, v92, v93
	v_cvt_pk_bf16_f32 v133, v94, v95
	s_mov_b64 s[4:5], -1
	s_and_b64 vcc, exec, s[8:9]
	s_cbranch_vccz .LBB0_618
	s_waitcnt vmcnt(0) lgkmcnt(0)
	s_barrier
	s_cbranch_execz .LBB0_619
